# k2shortpro
# speedup vs baseline: 1.0208x; 1.0208x over previous
_Z11attn_kernelILi4EEvPKfS1_S1_S1_S1_S1_PKcPf:
	s_load_dwordx2 s[24:25], s[0:1], 0x30
	s_load_dwordx8 s[8:15], s[0:1], 0x0
	s_load_dwordx4 s[16:19], s[0:1], 0x20
	v_lshrrev_b32_e32 v63, 6, v0
	v_and_b32_e32 v57, 15, v0
	v_bfe_u32 v1, v0, 4, 2
	s_lshl_b32 s26, s2, 8
	s_lshl_b32 s27, s2, 9
	v_lshrrev_b32_e32 v2, 2, v57
	v_mul_u32_u24_e32 v4, 3, v1
	s_add_u32 s26, s26, 0x164000
	s_add_u32 s27, s27, 0x80000
	v_mul_u32_u24_e32 v2, 3, v2
	v_mad_u32_u24 v4, v63, 12, v4
	s_add_u32 s20, s26, 0xc0
	v_mad_u32_u24 v2, v63, 12, v2
	v_lshlrev_b32_e32 v60, 5, v57
	v_lshlrev_b32_e32 v58, 3, v1
	v_lshl_add_u32 v4, v4, 2, s26
	v_lshl_add_u32 v2, v2, 2, s26
	v_add3_u32 v3, v60, v58, s27
	s_waitcnt lgkmcnt(0)
	global_load_dwordx3 v[80:82], v2, s[24:25]
	global_load_dwordx3 v[84:86], v4, s[24:25]
	global_load_dwordx2 v[64:65], v3, s[24:25]
	s_load_dword s3, s[24:25], s20
	v_and_b32_e32 v104, 63, v0
	v_lshrrev_b32_e32 v56, 4, v0
	v_lshlrev_b32_e32 v54, 4, v57
	v_mov_b32_e32 v59, 0
	s_movk_i32 s4, 0xe0
	v_cmp_gt_u32_e64 s[4:5], s4, v0
	s_mul_i32 s28, s2, 14
	v_lshlrev_b32_e32 v5, 2, v57
	v_lshlrev_b32_e32 v147, 6, v57
	v_mul_u32_u24_e32 v156, 0x140, v1
	s_movk_i32 s21, 0x500
	v_mad_u32_u24 v156, v63, s21, v156
	v_lshl_or_b32 v156, v57, 2, v156
	v_add_u32_e32 v156, 0x1c00, v156
	v_lshlrev_b32_e32 v157, 5, v56
	v_cmp_gt_u32_e32 vcc, 3, v57
	v_add_u32_e32 v158, 4, v57
	v_lshlrev_b32_e32 v159, 2, v57
	s_movk_i32 s21, 0x50
	v_cndmask_b32_e32 v158, 4, v158, vcc
	v_mad_u32_u24 v159, v56, s21, v159
	v_lshl_add_u32 v158, v158, 2, v157
	v_mul_u32_u24_e32 v250, 0x50, v56
	v_or_b32_e32 v250, 0x3800, v250
	v_lshl_add_u32 v251, v57, 1, v250
	v_mul_u32_u24_e32 v252, 0x50, v57
	v_lshl_add_u32 v252, v58, 1, v252
	v_lshlrev_b32_e32 v253, 2, v57
	v_and_b32_e32 v254, 0xc0, v0
	v_lshlrev_b32_e32 v255, 11, v1
	v_or3_b32 v253, v253, v254, v255
	v_add_u32_e32 v254, s28, v56
	v_lshl_add_u32 v254, v254, 9, v54
	v_lshl_or_b32 v255, v56, 9, v54
	s_add_u32 s22, s24, 0x160000
	s_addc_u32 s23, s25, 0
	v_cndmask_b32_e64 v62, 13, v56, s[4:5]
	v_add_u32_e32 v3, s28, v62
	v_mad_u32_u24 v144, v3, 36, v5
	v_mad_u32_u24 v146, v3, 12, v5
	v_add_u32_e32 v145, -36, v146
	v_add_u32_e32 v146, -48, v146
	v_lshl_or_b32 v147, v63, 10, v147
	v_lshl_or_b32 v147, v1, 4, v147
	v_or_b32_e32 v148, 0x1000, v147
	v_lshlrev_b32_e32 v149, 4, v104
	v_lshlrev_b32_e32 v150, 9, v3
	v_add_u32_e32 v150, v150, v54
	v_and_b32_e32 v87, 3, v57
	v_lshlrev_b32_e32 v87, 4, v87
	v_lshl_or_b32 v87, v1, 6, v87
	v_lshlrev_b32_e32 v88, 3, v57
	s_add_u32 s26, s24, 0x100000
	s_addc_u32 s27, s25, 0
	s_add_u32 s28, s24, 0x140000
	s_addc_u32 s29, s25, 0
	s_movk_i32 s6, 0x140
	v_cmp_gt_u32_e32 vcc, s6, v0
	v_lshlrev_b32_e32 v22, 2, v0
	v_mov_b32_e32 v23, 0
	s_and_saveexec_b64 s[6:7], vcc
	ds_write_b32 v22, v23 offset:14336
	s_or_b64 exec, exec, s[6:7]
	v_cmp_gt_u32_e32 vcc, 64, v0
	s_and_saveexec_b64 s[6:7], vcc
	ds_write_b32 v22, v23 offset:15360
	s_or_b64 exec, exec, s[6:7]
	v_mov_b32_e32 v45, 0xc9c35000
	s_mov_b32 s30, 0x3db8aa3b
	s_mov_b32 s31, 0x3db8aa3b
	v_mov_b32_e32 v121, 0x3fb8aa3b
	v_mov_b32_e32 v35, 0
	v_mov_b32_e32 v44, v45
	s_waitcnt lgkmcnt(0)
	s_bitcmp0_b32 s3, 1
	s_cselect_b64 s[20:21], -1, 0
	s_cbranch_scc1 .LBB1_16
	v_bfe_u32 v46, s3, v57, 1
	v_cmp_eq_u32_e32 vcc, 0, v46
	s_nop 1
	v_cndmask_b32_e32 v47, 0, v45, vcc
	v_cndmask_b32_e64 v55, 1.0, 0, vcc
	s_nop 0
	v_mov_b32_dpp v34, v47 row_newbcast:0 row_mask:0xf bank_mask:0xf bound_ctrl:1
	v_mov_b32_dpp v36, v47 row_newbcast:2 row_mask:0xf bank_mask:0xf bound_ctrl:1
	v_mov_b32_dpp v37, v47 row_newbcast:3 row_mask:0xf bank_mask:0xf bound_ctrl:1
	v_mov_b32_dpp v22, v47 row_newbcast:4 row_mask:0xf bank_mask:0xf bound_ctrl:1
	v_mov_b32_dpp v23, v47 row_newbcast:5 row_mask:0xf bank_mask:0xf bound_ctrl:1
	v_mov_b32_dpp v24, v47 row_newbcast:6 row_mask:0xf bank_mask:0xf bound_ctrl:1
	v_mov_b32_dpp v25, v47 row_newbcast:7 row_mask:0xf bank_mask:0xf bound_ctrl:1
	v_mov_b32_dpp v38, v47 row_newbcast:8 row_mask:0xf bank_mask:0xf bound_ctrl:1
	v_mov_b32_dpp v39, v47 row_newbcast:9 row_mask:0xf bank_mask:0xf bound_ctrl:1
	v_mov_b32_dpp v40, v47 row_newbcast:10 row_mask:0xf bank_mask:0xf bound_ctrl:1
	v_mov_b32_dpp v41, v47 row_newbcast:11 row_mask:0xf bank_mask:0xf bound_ctrl:1
	v_mov_b32_dpp v42, v47 row_newbcast:12 row_mask:0xf bank_mask:0xf bound_ctrl:1
	v_mov_b32_dpp v43, v47 row_newbcast:13 row_mask:0xf bank_mask:0xf bound_ctrl:1
	s_waitcnt vmcnt(1)
	v_lshl_add_u32 v72, v80, 9, v87
	v_lshl_add_u32 v73, v81, 9, v87
	v_lshl_add_u32 v74, v82, 9, v87
	global_load_dwordx4 v[50:53], v72, s[24:25]
	global_load_dwordx4 v[46:49], v72, s[24:25] offset:256
	global_load_dwordx4 v[14:17], v73, s[24:25]
	global_load_dwordx4 v[10:13], v73, s[24:25] offset:256
	global_load_dwordx4 v[6:9], v74, s[24:25]
	global_load_dwordx4 v[2:5], v74, s[24:25] offset:256
	v_lshl_add_u32 v75, v84, 8, v54
	v_lshl_add_u32 v78, v84, 7, v88
	v_lshl_add_u32 v76, v85, 8, v54
	v_lshl_add_u32 v79, v85, 7, v88
	v_lshl_add_u32 v77, v86, 8, v54
	v_lshl_add_u32 v80, v86, 7, v88
	global_load_dwordx4 v[30:33], v75, s[26:27]
	global_load_dwordx2 v[70:71], v78, s[28:29]
	global_load_dwordx4 v[26:29], v76, s[26:27]
	global_load_dwordx2 v[66:67], v79, s[28:29]
	global_load_dwordx4 v[18:21], v77, s[26:27]
	global_load_dwordx2 v[68:69], v80, s[28:29]
	s_mov_b32 exec_lo, 0x1ff01ff
	s_mov_b32 exec_hi, 0x1ff01ff
	global_load_dword v120, v144, s[10:11]
	s_mov_b32 exec_lo, 0xe000e00
	s_mov_b32 exec_hi, 0xe000e00
	global_load_dword v120, v145, s[12:13]
	s_mov_b32 exec_lo, 0x70007000
	s_mov_b32 exec_hi, 0x70007000
	global_load_dword v120, v146, s[14:15]
	s_mov_b64 exec, -1
	global_load_dwordx4 v[124:127], v147, s[22:23]
	global_load_dwordx4 v[128:131], v148, s[22:23]
	s_mov_b32 exec_hi, 0
	global_load_dwordx4 v[132:135], v149, s[16:17]
	s_mov_b32 exec_hi, -1
	s_mov_b32 exec_lo, 0
	global_load_dwordx4 v[132:135], v149, s[18:19] offset:-512
	s_mov_b32 exec_lo, -1
	global_load_dwordx4 v[136:139], v150, s[8:9]
	global_load_dwordx4 v[140:143], v150, s[8:9] offset:256
	v_mov_b32_e32 v75, 0
	v_mov_b32_e32 v79, 0
	v_mov_b32_e32 v83, 0
	s_waitcnt vmcnt(20)
	v_mfma_f32_16x16x32_fp8_fp8 v[160:163], v[50:51], v[64:65], v[34:37]
	v_mfma_f32_16x16x32_fp8_fp8 v[164:167], v[52:53], v[64:65], v[22:25]
	s_waitcnt vmcnt(19)
	v_mfma_f32_16x16x32_fp8_fp8 v[168:171], v[46:47], v[64:65], v[38:41]
	v_mfma_f32_16x16x32_fp8_fp8 v[172:175], v[48:49], v[64:65], v[42:45]
	s_nop 3
	v_max3_f32 v86, v160, v161, v162
	v_max3_f32 v87, v163, v164, v165
	v_max3_f32 v88, v166, v167, v168
	v_max3_f32 v89, v169, v170, v171
	v_max3_f32 v86, v86, v172, v173
	v_max3_f32 v87, v87, v88, v89
	v_max_f32_e32 v96, v86, v87
	v_mul_f32_e32 v98, 0xbdb8aa3b, v96
	v_pk_fma_f32 v[208:209], v[160:161], s[30:31], v[98:99] op_sel_hi:[1,1,0]
	v_pk_fma_f32 v[210:211], v[162:163], s[30:31], v[98:99] op_sel_hi:[1,1,0]
	v_pk_fma_f32 v[212:213], v[164:165], s[30:31], v[98:99] op_sel_hi:[1,1,0]
	v_pk_fma_f32 v[214:215], v[166:167], s[30:31], v[98:99] op_sel_hi:[1,1,0]
	v_pk_fma_f32 v[216:217], v[168:169], s[30:31], v[98:99] op_sel_hi:[1,1,0]
	v_pk_fma_f32 v[218:219], v[170:171], s[30:31], v[98:99] op_sel_hi:[1,1,0]
	v_pk_fma_f32 v[220:221], v[172:173], s[30:31], v[98:99] op_sel_hi:[1,1,0]
	v_exp_f32_e32 v208, v208
	v_exp_f32_e32 v209, v209
	v_exp_f32_e32 v210, v210
	v_exp_f32_e32 v211, v211
	v_exp_f32_e32 v212, v212
	v_exp_f32_e32 v213, v213
	v_exp_f32_e32 v214, v214
	v_exp_f32_e32 v215, v215
	v_exp_f32_e32 v216, v216
	v_exp_f32_e32 v217, v217
	v_exp_f32_e32 v218, v218
	v_exp_f32_e32 v219, v219
	v_exp_f32_e32 v220, v220
	v_exp_f32_e32 v221, v221
	s_waitcnt vmcnt(18)
	v_mfma_f32_16x16x32_fp8_fp8 v[176:179], v[14:15], v[64:65], v[34:37]
	v_mfma_f32_16x16x32_fp8_fp8 v[180:183], v[16:17], v[64:65], v[22:25]
	s_waitcnt vmcnt(17)
	v_mfma_f32_16x16x32_fp8_fp8 v[184:187], v[10:11], v[64:65], v[38:41]
	v_mfma_f32_16x16x32_fp8_fp8 v[188:191], v[12:13], v[64:65], v[42:45]
	v_pk_add_f32 v[86:87], v[208:209], v[210:211]
	v_pk_add_f32 v[88:89], v[212:213], v[214:215]
	v_pk_add_f32 v[90:91], v[216:217], v[218:219]
	v_pk_mul_f32 v[92:93], v[208:209], v[160:161]
	v_pk_mul_f32 v[94:95], v[210:211], v[162:163]
	v_pk_add_f32 v[86:87], v[86:87], v[220:221]
	v_pk_add_f32 v[88:89], v[88:89], v[90:91]
	v_pk_fma_f32 v[92:93], v[212:213], v[164:165], v[92:93]
	v_pk_fma_f32 v[94:95], v[214:215], v[166:167], v[94:95]
	v_pk_add_f32 v[86:87], v[86:87], v[88:89]
	v_pk_fma_f32 v[92:93], v[216:217], v[168:169], v[92:93]
	v_pk_fma_f32 v[94:95], v[218:219], v[170:171], v[94:95]
	v_add_f32_e32 v86, v86, v87
	v_pk_fma_f32 v[92:93], v[220:221], v[172:173], v[92:93]
	v_rcp_f32_e32 v87, v86
	v_pk_add_f32 v[92:93], v[92:93], v[94:95]
	v_mul_f32_e32 v87, v55, v87
	v_add_f32_e32 v92, v92, v93
	v_mul_f32_e32 v107, v86, v87
	v_mul_f32_e32 v92, v92, v87
	v_mul_f32_e32 v100, 0x43800000, v87
	v_mul_f32_e32 v103, 0x3d800000, v92
	v_max3_f32 v86, v176, v177, v178
	v_max3_f32 v87, v179, v180, v181
	v_max3_f32 v88, v182, v183, v184
	v_max3_f32 v89, v185, v186, v187
	v_max3_f32 v86, v86, v188, v189
	v_max3_f32 v87, v87, v88, v89
	v_max_f32_e32 v96, v86, v87
	v_mul_f32_e32 v98, 0xbdb8aa3b, v96
	v_pk_fma_f32 v[222:223], v[176:177], s[30:31], v[98:99] op_sel_hi:[1,1,0]
	v_pk_fma_f32 v[224:225], v[178:179], s[30:31], v[98:99] op_sel_hi:[1,1,0]
	v_pk_fma_f32 v[226:227], v[180:181], s[30:31], v[98:99] op_sel_hi:[1,1,0]
	v_pk_fma_f32 v[228:229], v[182:183], s[30:31], v[98:99] op_sel_hi:[1,1,0]
	v_pk_fma_f32 v[230:231], v[184:185], s[30:31], v[98:99] op_sel_hi:[1,1,0]
	v_pk_fma_f32 v[232:233], v[186:187], s[30:31], v[98:99] op_sel_hi:[1,1,0]
	v_pk_fma_f32 v[234:235], v[188:189], s[30:31], v[98:99] op_sel_hi:[1,1,0]
	v_exp_f32_e32 v222, v222
	v_exp_f32_e32 v223, v223
	v_exp_f32_e32 v224, v224
	v_exp_f32_e32 v225, v225
	v_exp_f32_e32 v226, v226
	v_exp_f32_e32 v227, v227
	v_exp_f32_e32 v228, v228
	v_exp_f32_e32 v229, v229
	v_exp_f32_e32 v230, v230
	v_exp_f32_e32 v231, v231
	v_exp_f32_e32 v232, v232
	v_exp_f32_e32 v233, v233
	v_exp_f32_e32 v234, v234
	v_exp_f32_e32 v235, v235
	s_waitcnt vmcnt(16)
	v_mfma_f32_16x16x32_fp8_fp8 v[192:195], v[6:7], v[64:65], v[34:37]
	v_mfma_f32_16x16x32_fp8_fp8 v[196:199], v[8:9], v[64:65], v[22:25]
	s_waitcnt vmcnt(15)
	v_mfma_f32_16x16x32_fp8_fp8 v[200:203], v[2:3], v[64:65], v[38:41]
	v_mfma_f32_16x16x32_fp8_fp8 v[204:207], v[4:5], v[64:65], v[42:45]
	v_pk_add_f32 v[86:87], v[222:223], v[224:225]
	v_pk_add_f32 v[88:89], v[226:227], v[228:229]
	v_pk_add_f32 v[90:91], v[230:231], v[232:233]
	v_pk_mul_f32 v[92:93], v[222:223], v[176:177]
	v_pk_mul_f32 v[94:95], v[224:225], v[178:179]
	v_pk_add_f32 v[86:87], v[86:87], v[234:235]
	v_pk_add_f32 v[88:89], v[88:89], v[90:91]
	v_pk_fma_f32 v[92:93], v[226:227], v[180:181], v[92:93]
	v_pk_fma_f32 v[94:95], v[228:229], v[182:183], v[94:95]
	v_pk_add_f32 v[86:87], v[86:87], v[88:89]
	v_pk_fma_f32 v[92:93], v[230:231], v[184:185], v[92:93]
	v_pk_fma_f32 v[94:95], v[232:233], v[186:187], v[94:95]
	v_add_f32_e32 v86, v86, v87
	v_pk_fma_f32 v[92:93], v[234:235], v[188:189], v[92:93]
	v_rcp_f32_e32 v87, v86
	v_pk_add_f32 v[92:93], v[92:93], v[94:95]
	v_mul_f32_e32 v87, v55, v87
	v_add_f32_e32 v92, v92, v93
	v_mul_f32_e32 v108, v86, v87
	v_mul_f32_e32 v92, v92, v87
	v_mul_f32_e32 v101, 0x43800000, v87
	v_mul_f32_e32 v105, 0x3d800000, v92
	v_max3_f32 v86, v192, v193, v194
	v_max3_f32 v87, v195, v196, v197
	v_max3_f32 v88, v198, v199, v200
	v_max3_f32 v89, v201, v202, v203
	v_max3_f32 v86, v86, v204, v205
	v_max3_f32 v87, v87, v88, v89
	v_max_f32_e32 v96, v86, v87
	v_mul_f32_e32 v98, 0xbdb8aa3b, v96
	v_pk_fma_f32 v[236:237], v[192:193], s[30:31], v[98:99] op_sel_hi:[1,1,0]
	v_pk_fma_f32 v[238:239], v[194:195], s[30:31], v[98:99] op_sel_hi:[1,1,0]
	v_pk_fma_f32 v[240:241], v[196:197], s[30:31], v[98:99] op_sel_hi:[1,1,0]
	v_pk_fma_f32 v[242:243], v[198:199], s[30:31], v[98:99] op_sel_hi:[1,1,0]
	v_pk_fma_f32 v[244:245], v[200:201], s[30:31], v[98:99] op_sel_hi:[1,1,0]
	v_pk_fma_f32 v[246:247], v[202:203], s[30:31], v[98:99] op_sel_hi:[1,1,0]
	v_pk_fma_f32 v[248:249], v[204:205], s[30:31], v[98:99] op_sel_hi:[1,1,0]
	v_exp_f32_e32 v236, v236
	v_exp_f32_e32 v237, v237
	v_exp_f32_e32 v238, v238
	v_exp_f32_e32 v239, v239
	v_exp_f32_e32 v240, v240
	v_exp_f32_e32 v241, v241
	v_exp_f32_e32 v242, v242
	v_exp_f32_e32 v243, v243
	v_exp_f32_e32 v244, v244
	v_exp_f32_e32 v245, v245
	v_exp_f32_e32 v246, v246
	v_exp_f32_e32 v247, v247
	v_exp_f32_e32 v248, v248
	v_exp_f32_e32 v249, v249
	v_pk_add_f32 v[86:87], v[236:237], v[238:239]
	v_pk_add_f32 v[88:89], v[240:241], v[242:243]
	v_pk_add_f32 v[90:91], v[244:245], v[246:247]
	v_pk_mul_f32 v[92:93], v[236:237], v[192:193]
	v_pk_mul_f32 v[94:95], v[238:239], v[194:195]
	v_pk_add_f32 v[86:87], v[86:87], v[248:249]
	v_pk_add_f32 v[88:89], v[88:89], v[90:91]
	v_pk_fma_f32 v[92:93], v[240:241], v[196:197], v[92:93]
	v_pk_fma_f32 v[94:95], v[242:243], v[198:199], v[94:95]
	v_pk_add_f32 v[86:87], v[86:87], v[88:89]
	v_pk_fma_f32 v[92:93], v[244:245], v[200:201], v[92:93]
	v_pk_fma_f32 v[94:95], v[246:247], v[202:203], v[94:95]
	v_add_f32_e32 v86, v86, v87
	v_pk_fma_f32 v[92:93], v[248:249], v[204:205], v[92:93]
	v_rcp_f32_e32 v87, v86
	v_pk_add_f32 v[92:93], v[92:93], v[94:95]
	v_mul_f32_e32 v87, v55, v87
	v_add_f32_e32 v92, v92, v93
	v_mul_f32_e32 v109, v86, v87
	v_mul_f32_e32 v92, v92, v87
	v_mul_f32_e32 v102, 0x43800000, v87
	v_mul_f32_e32 v106, 0x3d800000, v92
	v_max3_f32 v122, v103, v105, v106
	v_cmp_gt_u32_e64 s[6:7], 16, v104
	v_mov_b32_e32 v123, v122
	s_nop 1
	v_permlane16_swap_b32_e32 v122, v123
	v_max_f32_e32 v122, v122, v123
	v_mov_b32_e32 v123, v122
	s_nop 1
	v_permlane32_swap_b32_e32 v122, v123
	v_max_f32_e32 v36, v122, v123
	v_mul_f32_e32 v123, 0x3fb8aa3b, v36
	v_fma_f32 v111, v103, v121, -v123
	v_exp_f32_e32 v111, v111
	s_nop 0
	v_mul_f32_e32 v112, v111, v100
	v_mul_f32_e32 v110, v111, v107
	v_mov_b32_e32 v114, v111
	v_pk_mul_f32 v[208:209], v[208:209], v[112:113] op_sel_hi:[1,0]
	v_pk_mul_f32 v[210:211], v[210:211], v[112:113] op_sel_hi:[1,0]
	v_pk_mul_f32 v[212:213], v[212:213], v[112:113] op_sel_hi:[1,0]
	v_pk_mul_f32 v[214:215], v[214:215], v[112:113] op_sel_hi:[1,0]
	v_pk_mul_f32 v[216:217], v[216:217], v[112:113] op_sel_hi:[1,0]
	v_pk_mul_f32 v[218:219], v[218:219], v[112:113] op_sel_hi:[1,0]
	v_pk_mul_f32 v[220:221], v[220:221], v[112:113] op_sel_hi:[1,0]
	s_waitcnt vmcnt(13)
	v_mov_b32_e32 v115, v110
	v_fma_mix_f32 v116, v110, v70, 0 op_sel_hi:[0,1,0]
	v_fma_mix_f32 v117, v110, v70, 0 op_sel:[0,1,0] op_sel_hi:[0,1,0]
	v_fma_mix_f32 v118, v110, v71, 0 op_sel_hi:[0,1,0]
	v_cvt_pk_fp8_f32 v72, v208, v209
	v_cvt_pk_fp8_f32 v73, v212, v213
	v_cvt_pk_fp8_f32 v74, v216, v217
	v_cvt_pk_fp8_f32 v75, v220, v221
	v_cvt_pk_fp8_f32 v72, v210, v211 op_sel:[0,0,1]
	v_cvt_pk_fp8_f32 v73, v214, v215 op_sel:[0,0,1]
	v_cvt_pk_fp8_f32 v74, v218, v219 op_sel:[0,0,1]
	s_nop 1
	v_mfma_f32_16x16x32_fp8_fp8 v[152:155], v[72:73], v[30:31], 0
	v_mfma_f32_16x16x32_fp8_fp8 v[152:155], v[74:75], v[32:33], v[152:155]
	v_fma_f32 v111, v105, v121, -v123
	v_exp_f32_e32 v111, v111
	s_nop 0
	v_mul_f32_e32 v112, v111, v101
	v_mul_f32_e32 v110, v111, v108
	v_add_f32_e32 v114, v114, v111
	v_pk_mul_f32 v[222:223], v[222:223], v[112:113] op_sel_hi:[1,0]
	v_pk_mul_f32 v[224:225], v[224:225], v[112:113] op_sel_hi:[1,0]
	v_pk_mul_f32 v[226:227], v[226:227], v[112:113] op_sel_hi:[1,0]
	v_pk_mul_f32 v[228:229], v[228:229], v[112:113] op_sel_hi:[1,0]
	v_pk_mul_f32 v[230:231], v[230:231], v[112:113] op_sel_hi:[1,0]
	v_pk_mul_f32 v[232:233], v[232:233], v[112:113] op_sel_hi:[1,0]
	v_pk_mul_f32 v[234:235], v[234:235], v[112:113] op_sel_hi:[1,0]
	s_waitcnt vmcnt(11)
	v_add_f32_e32 v115, v115, v110
	v_fma_mix_f32 v116, v110, v66, v116 op_sel_hi:[0,1,0]
	v_fma_mix_f32 v117, v110, v66, v117 op_sel:[0,1,0] op_sel_hi:[0,1,0]
	v_fma_mix_f32 v118, v110, v67, v118 op_sel_hi:[0,1,0]
	v_cvt_pk_fp8_f32 v76, v222, v223
	v_cvt_pk_fp8_f32 v77, v226, v227
	v_cvt_pk_fp8_f32 v78, v230, v231
	v_cvt_pk_fp8_f32 v79, v234, v235
	v_cvt_pk_fp8_f32 v76, v224, v225 op_sel:[0,0,1]
	v_cvt_pk_fp8_f32 v77, v228, v229 op_sel:[0,0,1]
	v_cvt_pk_fp8_f32 v78, v232, v233 op_sel:[0,0,1]
	s_nop 1
	v_mfma_f32_16x16x32_fp8_fp8 v[152:155], v[76:77], v[26:27], v[152:155]
	v_mfma_f32_16x16x32_fp8_fp8 v[152:155], v[78:79], v[28:29], v[152:155]
	v_fma_f32 v111, v106, v121, -v123
	v_exp_f32_e32 v111, v111
	s_nop 0
	v_mul_f32_e32 v112, v111, v102
	v_mul_f32_e32 v110, v111, v109
	v_add_f32_e32 v114, v114, v111
	v_pk_mul_f32 v[236:237], v[236:237], v[112:113] op_sel_hi:[1,0]
	v_pk_mul_f32 v[238:239], v[238:239], v[112:113] op_sel_hi:[1,0]
	v_pk_mul_f32 v[240:241], v[240:241], v[112:113] op_sel_hi:[1,0]
	v_pk_mul_f32 v[242:243], v[242:243], v[112:113] op_sel_hi:[1,0]
	v_pk_mul_f32 v[244:245], v[244:245], v[112:113] op_sel_hi:[1,0]
	v_pk_mul_f32 v[246:247], v[246:247], v[112:113] op_sel_hi:[1,0]
	v_pk_mul_f32 v[248:249], v[248:249], v[112:113] op_sel_hi:[1,0]
	s_waitcnt vmcnt(9)
	v_add_f32_e32 v115, v115, v110
	v_fma_mix_f32 v116, v110, v68, v116 op_sel_hi:[0,1,0]
	v_fma_mix_f32 v117, v110, v68, v117 op_sel:[0,1,0] op_sel_hi:[0,1,0]
	v_fma_mix_f32 v118, v110, v69, v118 op_sel_hi:[0,1,0]
	v_cvt_pk_fp8_f32 v80, v236, v237
	v_cvt_pk_fp8_f32 v81, v240, v241
	v_cvt_pk_fp8_f32 v82, v244, v245
	v_cvt_pk_fp8_f32 v83, v248, v249
	v_cvt_pk_fp8_f32 v80, v238, v239 op_sel:[0,0,1]
	v_cvt_pk_fp8_f32 v81, v242, v243 op_sel:[0,0,1]
	v_cvt_pk_fp8_f32 v82, v246, v247 op_sel:[0,0,1]
	s_nop 1
	v_mfma_f32_16x16x32_fp8_fp8 v[152:155], v[80:81], v[18:19], v[152:155]
	v_mfma_f32_16x16x32_fp8_fp8 v[152:155], v[82:83], v[20:21], v[152:155]
	v_mov_b32_e32 v86, v114
	v_mov_b32_e32 v87, v115
	v_mov_b32_e32 v88, v116
	v_mov_b32_e32 v89, v117
	v_mov_b32_e32 v90, v118
	v_permlane16_swap_b32_e32 v114, v86
	v_permlane16_swap_b32_e32 v115, v87
	v_permlane16_swap_b32_e32 v116, v88
	v_permlane16_swap_b32_e32 v117, v89
	v_permlane16_swap_b32_e32 v118, v90
	v_add_f32_e32 v114, v114, v86
	v_add_f32_e32 v115, v115, v87
	v_add_f32_e32 v116, v116, v88
	v_add_f32_e32 v117, v117, v89
	v_add_f32_e32 v118, v118, v90
	v_mov_b32_e32 v86, v114
	v_mov_b32_e32 v87, v115
	v_mov_b32_e32 v88, v116
	v_mov_b32_e32 v89, v117
	v_mov_b32_e32 v90, v118
	v_permlane32_swap_b32_e32 v114, v86
	v_permlane32_swap_b32_e32 v115, v87
	v_permlane32_swap_b32_e32 v116, v88
	v_permlane32_swap_b32_e32 v117, v89
	v_permlane32_swap_b32_e32 v118, v90
	v_add_f32_e32 v37, v114, v86
	v_add_f32_e32 v20, v115, v87
	v_add_f32_e32 v18, v116, v88
	v_add_f32_e32 v19, v117, v89
	v_add_f32_e32 v21, v118, v90
	ds_write2_b32 v156, v152, v153 offset0:0 offset1:20
	ds_write2_b32 v156, v154, v155 offset0:40 offset1:60
	s_branch .LBB1_30
